# attention: the 7 ring LDS-DMA pieces of a step issued one per gap between the 8 P.V MFMAs (common case), row-max under the P.V MFMAs (on v11)
# speedup vs baseline: 1.0022x; 1.0022x over previous
; #define ATT_DMAK(tile, slot) do { _Pragma("unroll") for (int i = 0; i < 4; ++i) { const int pc = (wv + 8 * i) < 25 ? (wv + 8 * i) : 24; \
;         __builtin_amdgcn_global_load_lds((const unsigned*)((const char*)Kbh + (size_t)(tile) * (64 * 384) + doffK[i]), (LAS unsigned*)(lds + (slot) * KT_BYTES + pc * 1024), 16, 0, 0); } } while (0)
; #define ATT_DMAV(tile, slot) do { _Pragma("unroll") for (int i = 0; i < 3; ++i) { const int pc = (wv + 8 * i) < 18 ? (wv + 8 * i) : 17; \
;         __builtin_amdgcn_global_load_lds((const unsigned*)((const char*)Vbh + (size_t)(tile) * 128 + doffV[i]), (LAS unsigned*)(lds + VRING + (slot) * VT_BYTES + pc * 1024), 16, 0, 0); } } while (0)
; __device__ __forceinline__ void attn_unit(const bf16_t* Qrows  , const bf16_t* Kbh, const bf16_t* Vbh, int nkeys, bf16_t* Orows, LAS unsigned char* lds) {
;     ...
;         if (j + 4 < nt) ATT_DMAK(j + 4, v0);
;         if (j + 3 < nt) ATT_DMAV(j + 3, v0 == 0 ? 2 : v0 - 1);
.LBB0_1235:
	s_add_i32 s15, s14, 1
	s_cmp_lg_u32 s14, 2
	s_cselect_b32 s14, s15, 0
	s_mul_i32 s15, s14, 0x6400
	v_add_u32_e32 v70, s15, v185
	ds_read_b128 v[66:69], v70
	ds_read_b128 v[166:169], v70 offset:32
	ds_read_b128 v[170:173], v70 offset:64
	ds_read_b128 v[188:191], v70 offset:96
	ds_read_b128 v[192:195], v70 offset:128
	ds_read_b128 v[196:199], v70 offset:160
	ds_read_b128 v[200:203], v70 offset:192
	ds_read_b128 v[216:219], v70 offset:224
	ds_read_b128 v[220:223], v70 offset:256
	ds_read_b128 v[224:227], v70 offset:288
	ds_read_b128 v[228:231], v70 offset:320
	ds_read_b128 v[146:149], v70 offset:352
	s_waitcnt lgkmcnt(11)
	v_mfma_f32_32x32x16_bf16 v[66:81], v[66:69], v[142:145], 0
	v_sub_f32_e32 v82, v82, v183
	v_exp_f32_e32 v82, v82
	v_sub_f32_e32 v94, v94, v183
	v_exp_f32_e32 v94, v94
	v_add_f32_e32 v165, 0, v82
	v_add_f32_e32 v165, v94, v165
	s_waitcnt lgkmcnt(10)
	v_mfma_f32_32x32x16_bf16 v[66:81], v[166:169], v[138:141], v[66:81]
	v_sub_f32_e32 v83, v83, v183
	v_exp_f32_e32 v83, v83
	v_sub_f32_e32 v95, v95, v183
	v_exp_f32_e32 v95, v95
	v_add_f32_e32 v165, v83, v165
	v_cvt_pk_bf16_f32 v82, v82, v83
	v_add_f32_e32 v165, v95, v165
	v_sub_f32_e32 v83, v84, v183
	s_waitcnt lgkmcnt(9)
	v_mfma_f32_32x32x16_bf16 v[66:81], v[170:173], v[134:137], v[66:81]
	v_exp_f32_e32 v83, v83
	v_sub_f32_e32 v96, v96, v183
	v_add_f32_e32 v84, v83, v165
	v_exp_f32_e32 v165, v96
	s_nop 0
	v_add_f32_e32 v84, v165, v84
	s_waitcnt lgkmcnt(8)
	v_mfma_f32_32x32x16_bf16 v[66:81], v[188:191], v[130:133], v[66:81]
	v_sub_f32_e32 v85, v85, v183
	v_exp_f32_e32 v85, v85
	v_sub_f32_e32 v96, v97, v183
	v_exp_f32_e32 v97, v96
	v_cvt_pk_bf16_f32 v96, v94, v95
	v_add_f32_e32 v84, v85, v84
	v_cvt_pk_bf16_f32 v83, v83, v85
	v_add_f32_e32 v84, v97, v84
	v_cvt_pk_bf16_f32 v97, v165, v97
	s_waitcnt lgkmcnt(7)
	v_mfma_f32_32x32x16_bf16 v[66:81], v[192:195], v[126:129], v[66:81]
	v_sub_f32_e32 v85, v86, v183
	v_exp_f32_e32 v85, v85
	s_nop 0
	v_add_f32_e32 v84, v85, v84
	s_waitcnt lgkmcnt(6)
	v_mfma_f32_32x32x16_bf16 v[66:81], v[196:199], v[122:125], v[66:81]
	v_sub_f32_e32 v86, v87, v183
	v_exp_f32_e32 v86, v86
	s_nop 0
	v_add_f32_e32 v87, v86, v84
	v_cvt_pk_bf16_f32 v84, v85, v86
	s_waitcnt lgkmcnt(5)
	v_mfma_f32_32x32x16_bf16 v[66:81], v[200:203], v[118:121], v[66:81]
	v_sub_f32_e32 v85, v88, v183
	v_exp_f32_e32 v85, v85
	s_nop 0
	v_add_f32_e32 v86, v85, v87
	s_waitcnt lgkmcnt(4)
	v_mfma_f32_32x32x16_bf16 v[66:81], v[216:219], v[114:117], v[66:81]
	v_sub_f32_e32 v87, v89, v183
	v_exp_f32_e32 v87, v87
	s_nop 0
	v_add_f32_e32 v86, v87, v86
	v_cvt_pk_bf16_f32 v85, v85, v87
	v_sub_f32_e32 v87, v90, v183
	v_exp_f32_e32 v90, v87
	s_waitcnt lgkmcnt(3)
	v_mfma_f32_32x32x16_bf16 v[66:81], v[220:223], v[110:113], v[66:81]
	v_add_u32_e32 v165, s13, v187
	v_add_f32_e32 v94, v90, v86
	ds_read_b128 v[86:89], v165
	ds_read_b128 v[166:169], v165 offset:32
	s_waitcnt lgkmcnt(4)
	v_mfma_f32_32x32x16_bf16 v[66:81], v[224:227], v[106:109], v[66:81]
	v_sub_f32_e32 v91, v91, v183
	ds_read_b128 v[170:173], v165 offset:4608
	ds_read_b128 v[188:191], v165 offset:4640
	v_exp_f32_e32 v91, v91
	s_nop 0
	v_add_f32_e32 v95, v91, v94
	v_cvt_pk_bf16_f32 v94, v90, v91
	s_waitcnt lgkmcnt(5)
	v_mfma_f32_32x32x16_bf16 v[66:81], v[228:231], v[102:105], v[66:81]
	v_sub_f32_e32 v90, v92, v183
	ds_read_b128 v[192:195], v165 offset:9216
	ds_read_b128 v[196:199], v165 offset:9248
	v_exp_f32_e32 v90, v90
	s_nop 0
	v_add_f32_e32 v91, v90, v95
	v_sub_f32_e32 v92, v93, v183
	v_exp_f32_e32 v92, v92
	s_waitcnt lgkmcnt(6)
	v_mfma_f32_32x32x16_bf16 v[66:81], v[146:149], v[98:101], v[66:81]
	v_add_f32_e32 v186, v92, v91
	v_cvt_pk_bf16_f32 v95, v90, v92
	ds_read_b128 v[90:93], v165 offset:13824
	ds_read_b128 v[146:149], v165 offset:13856
	s_orn2_b64 vcc, s[0:1], s[24:25]
	s_and_b64 vcc, vcc, exec
	s_cbranch_vccnz .LattB_slow
	s_mul_i32 s13, s12, 0x6400
	s_add_u32 s16, s80, s2
	s_addc_u32 s17, s81, s3
	s_add_u32 s16, s16, 0x30e90000
	s_addc_u32 s17, s17, 0
	s_waitcnt lgkmcnt(0)
	v_mfma_f32_32x32x16_bf16 v[50:65], v[86:89], v[82:85], v[50:65]
	v_add_f32_e32 v186, v164, v186
	s_add_i32 m0, s13, s65
	s_nop 0
	global_load_lds_dwordx4 v208, s[16:17]
	v_mfma_f32_32x32x16_bf16 v[34:49], v[170:173], v[82:85], v[34:49]
	s_add_i32 m0, s13, s66
	s_nop 0
	global_load_lds_dwordx4 v209, s[16:17]
	v_mfma_f32_32x32x16_bf16 v[18:33], v[192:195], v[82:85], v[18:33]
	v_max_f32_e32 v150, v66, v67
	v_max3_f32 v150, v150, v68, v69
	s_add_i32 m0, s13, s67
	s_add_i32 s13, s13, s68
	global_load_lds_dwordx4 v210, s[16:17]
	v_mfma_f32_32x32x16_bf16 v[2:17], v[90:93], v[82:85], v[2:17]
	v_max3_f32 v150, v150, v70, v71
	v_max3_f32 v150, v150, v72, v73
	s_add_i32 m0, s13, 0x6000
	s_nop 0
	global_load_lds_dwordx4 v211, s[16:17]
	v_mfma_f32_32x32x16_bf16 v[50:65], v[166:169], v[94:97], v[50:65]
	v_max3_f32 v150, v150, v74, v75
	v_max3_f32 v150, v150, v76, v77
	s_mul_i32 s13, s12, 0x4800
	s_add_i32 s15, s13, 0xffffb800
	s_cmp_lg_u32 s12, 0
	s_cselect_b32 s15, s15, 0x9000
	s_add_i32 s15, s15, 0x12c00
	s_add_u32 s16, s82, s2
	s_addc_u32 s17, s83, s3
	s_add_u32 s16, s16, 0x31bf8180
	s_addc_u32 s17, s17, 0
	s_add_i32 m0, s15, s69
	s_nop 0
	global_load_lds_dwordx4 v212, s[16:17]
	v_mfma_f32_32x32x16_bf16 v[34:49], v[188:191], v[94:97], v[34:49]
	v_max3_f32 v150, v150, v78, v79
	v_max3_f32 v150, v150, v80, v81
	s_add_i32 m0, s15, s70
	s_nop 0
	global_load_lds_dwordx4 v213, s[16:17]
	v_mfma_f32_32x32x16_bf16 v[18:33], v[196:199], v[94:97], v[18:33]
	s_add_i32 m0, s15, s71
	s_nop 0
	global_load_lds_dwordx4 v214, s[16:17]
	v_mfma_f32_32x32x16_bf16 v[2:17], v[146:149], v[94:97], v[2:17]
	v_mov_b32_e32 v151, v150
	s_nop 1
	v_permlane32_swap_b32_e32 v151, v150
	v_max_f32_e32 v150, v150, v151
	s_branch .LattB_join
.LattB_slow:
	s_waitcnt lgkmcnt(0)
	v_mfma_f32_32x32x16_bf16 v[50:65], v[86:89], v[82:85], v[50:65]
	v_add_f32_e32 v186, v164, v186
	v_mfma_f32_32x32x16_bf16 v[34:49], v[170:173], v[82:85], v[34:49]
	v_mfma_f32_32x32x16_bf16 v[18:33], v[192:195], v[82:85], v[18:33]
	v_max_f32_e32 v150, v66, v67
	v_max3_f32 v150, v150, v68, v69
	v_mfma_f32_32x32x16_bf16 v[2:17], v[90:93], v[82:85], v[2:17]
	s_and_b64 vcc, exec, s[0:1]
	s_cbranch_vccnz .LattB_v
	s_mul_i32 s13, s12, 0x6400
	s_add_i32 s13, s13, 0
	s_add_u32 s16, s80, s2
	s_addc_u32 s17, s81, s3
	s_add_u32 s16, s16, 0x30e90000
	s_addc_u32 s17, s17, 0
	s_add_i32 m0, s13, s65
	s_nop 0
	global_load_lds_dwordx4 v208, s[16:17]
	s_add_i32 m0, s13, s66
	s_nop 0
	global_load_lds_dwordx4 v209, s[16:17]
	s_add_i32 m0, s13, s67
	s_add_i32 s13, s13, s68
	global_load_lds_dwordx4 v210, s[16:17]
	s_add_i32 m0, s13, 0x6000
	s_nop 0
	global_load_lds_dwordx4 v211, s[16:17]

; #define ATT_DMAK(tile, slot) do { _Pragma("unroll") for (int i = 0; i < 4; ++i) { const int pc = (wv + 8 * i) < 25 ? (wv + 8 * i) : 24; \
;         __builtin_amdgcn_global_load_lds((const unsigned*)((const char*)Kbh + (size_t)(tile) * (64 * 384) + doffK[i]), (LAS unsigned*)(lds + (slot) * KT_BYTES + pc * 1024), 16, 0, 0); } } while (0)
; #define ATT_DMAV(tile, slot) do { _Pragma("unroll") for (int i = 0; i < 3; ++i) { const int pc = (wv + 8 * i) < 18 ? (wv + 8 * i) : 17; \
;         __builtin_amdgcn_global_load_lds((const unsigned*)((const char*)Vbh + (size_t)(tile) * 128 + doffV[i]), (LAS unsigned*)(lds + VRING + (slot) * VT_BYTES + pc * 1024), 16, 0, 0); } } while (0)
; #define ATT_SYNC(full) do { if (full) asm volatile("s_waitcnt vmcnt(7)" ::: "memory"); else asm volatile("s_waitcnt vmcnt(0)" ::: "memory"); \
;         __builtin_amdgcn_s_barrier(); asm volatile("" ::: "memory"); } while (0)
; __device__ __forceinline__ void attn_unit(const bf16_t* Qrows  , const bf16_t* Kbh, const bf16_t* Vbh, int nkeys, bf16_t* Orows, LAS unsigned char* lds) {
;     ...
;         k1 = k1 == 2 ? 0 : k1 + 1; v0 = v0 == 2 ? 0 : v0 + 1;
;         ATT_SYNC(j + 3 < nt);
;         if (j + 4 < nt) ATT_DMAK(j + 4, v0);
;         if (j + 3 < nt) ATT_DMAV(j + 3, v0 == 0 ? 2 : v0 - 1);
;         ATT_STEP(sB, sA, true, k1, v0);
;         k1 = k1 == 2 ? 0 : k1 + 1; v0 = v0 == 2 ? 0 : v0 + 1;
;     }
.LattB_end:
.LattB_join:
	s_add_i32 s13, s14, 1
	s_cmp_lg_u32 s14, 2
	s_cselect_b32 s14, s13, 0
	s_add_i32 s13, s12, 1
	s_cmp_lg_u32 s12, 2
	s_cselect_b32 s36, s13, 0
	s_add_u32 s80, s80, s6
	s_addc_u32 s81, s81, s7
	s_add_u32 s82, s82, s10
	s_addc_u32 s83, s83, s11
	s_add_i32 s63, s63, 2
	s_andn2_b64 vcc, exec, s[0:1]
	s_cbranch_vccz .LBB0_1250

; #define ATT_DMAK(tile, slot) do { _Pragma("unroll") for (int i = 0; i < 4; ++i) { const int pc = (wv + 8 * i) < 25 ? (wv + 8 * i) : 24; \
;         __builtin_amdgcn_global_load_lds((const unsigned*)((const char*)Kbh + (size_t)(tile) * (64 * 384) + doffK[i]), (LAS unsigned*)(lds + (slot) * KT_BYTES + pc * 1024), 16, 0, 0); } } while (0)
; #define ATT_DMAV(tile, slot) do { _Pragma("unroll") for (int i = 0; i < 3; ++i) { const int pc = (wv + 8 * i) < 18 ? (wv + 8 * i) : 17; \
;         __builtin_amdgcn_global_load_lds((const unsigned*)((const char*)Vbh + (size_t)(tile) * 128 + doffV[i]), (LAS unsigned*)(lds + VRING + (slot) * VT_BYTES + pc * 1024), 16, 0, 0); } } while (0)
; __device__ __forceinline__ void attn_unit(const bf16_t* Qrows  , const bf16_t* Kbh, const bf16_t* Vbh, int nkeys, bf16_t* Orows, LAS unsigned char* lds) {
;     ...
;         if (j + 3 < nt) ATT_DMAK(j + 3, v0);
;         ATT_DMAV(j + 2, v0 == 0 ? 2 : v0 - 1);
.LBB0_1240:
	s_mul_i32 s13, s14, 0x6400
	v_add_u32_e32 v86, s13, v185
	ds_read_b128 v[82:85], v86
	ds_read_b128 v[188:191], v86 offset:32
	ds_read_b128 v[192:195], v86 offset:64
	ds_read_b128 v[196:199], v86 offset:96
	ds_read_b128 v[200:203], v86 offset:128
	ds_read_b128 v[216:219], v86 offset:160
	ds_read_b128 v[220:223], v86 offset:192
	ds_read_b128 v[224:227], v86 offset:224
	ds_read_b128 v[228:231], v86 offset:256
	ds_read_b128 v[232:235], v86 offset:288
	ds_read_b128 v[236:239], v86 offset:320
	ds_read_b128 v[240:243], v86 offset:352
	s_waitcnt lgkmcnt(11)
	v_mfma_f32_32x32x16_bf16 v[82:97], v[82:85], v[142:145], 0
	v_sub_f32_e32 v66, v66, v183
	v_sub_f32_e32 v78, v78, v183
	v_exp_f32_e32 v66, v66
	v_exp_f32_e32 v78, v78
	s_waitcnt lgkmcnt(10)
	v_mfma_f32_32x32x16_bf16 v[82:97], v[188:191], v[138:141], v[82:97]
	v_sub_f32_e32 v67, v67, v183
	v_sub_f32_e32 v79, v79, v183
	v_exp_f32_e32 v67, v67
	v_exp_f32_e32 v79, v79
	v_cvt_pk_bf16_f32 v188, v66, v67
	s_waitcnt lgkmcnt(9)
	v_mfma_f32_32x32x16_bf16 v[82:97], v[192:195], v[134:137], v[82:97]
	v_sub_f32_e32 v68, v68, v183
	v_sub_f32_e32 v80, v80, v183
	v_exp_f32_e32 v68, v68
	v_exp_f32_e32 v80, v80
	s_waitcnt lgkmcnt(8)
	v_mfma_f32_32x32x16_bf16 v[82:97], v[196:199], v[130:133], v[82:97]
	v_sub_f32_e32 v69, v69, v183
	v_sub_f32_e32 v81, v81, v183
	v_exp_f32_e32 v69, v69
	v_exp_f32_e32 v81, v81
	v_cvt_pk_bf16_f32 v194, v78, v79
	v_cvt_pk_bf16_f32 v189, v68, v69
	v_cvt_pk_bf16_f32 v195, v80, v81
	s_waitcnt lgkmcnt(7)
	v_mfma_f32_32x32x16_bf16 v[82:97], v[200:203], v[126:129], v[82:97]
	v_sub_f32_e32 v70, v70, v183
	v_exp_f32_e32 v70, v70
	s_waitcnt lgkmcnt(6)
	v_mfma_f32_32x32x16_bf16 v[82:97], v[216:219], v[122:125], v[82:97]
	v_sub_f32_e32 v71, v71, v183
	v_exp_f32_e32 v71, v71
	s_nop 0
	v_cvt_pk_bf16_f32 v190, v70, v71
	s_waitcnt lgkmcnt(5)
	v_mfma_f32_32x32x16_bf16 v[82:97], v[220:223], v[118:121], v[82:97]
	v_sub_f32_e32 v72, v72, v183
	v_exp_f32_e32 v72, v72
	s_waitcnt lgkmcnt(4)
	v_mfma_f32_32x32x16_bf16 v[82:97], v[224:227], v[114:117], v[82:97]
	v_sub_f32_e32 v73, v73, v183
	v_exp_f32_e32 v73, v73
	s_nop 0
	v_cvt_pk_bf16_f32 v191, v72, v73
	s_waitcnt lgkmcnt(3)
	v_mfma_f32_32x32x16_bf16 v[82:97], v[228:231], v[110:113], v[82:97]
	v_add_u32_e32 v204, s12, v187
	v_sub_f32_e32 v74, v74, v183
	ds_read_b128 v[196:199], v204
	ds_read_b128 v[200:203], v204 offset:32
	v_exp_f32_e32 v74, v74
	s_waitcnt lgkmcnt(4)
	v_mfma_f32_32x32x16_bf16 v[82:97], v[232:235], v[106:109], v[82:97]
	v_sub_f32_e32 v75, v75, v183
	ds_read_b128 v[216:219], v204 offset:4608
	ds_read_b128 v[220:223], v204 offset:4640
	v_exp_f32_e32 v75, v75
	s_nop 0
	v_cvt_pk_bf16_f32 v192, v74, v75
	s_waitcnt lgkmcnt(5)
	v_mfma_f32_32x32x16_bf16 v[82:97], v[236:239], v[102:105], v[82:97]
	v_sub_f32_e32 v76, v76, v183
	ds_read_b128 v[224:227], v204 offset:9216
	ds_read_b128 v[228:231], v204 offset:9248
	v_exp_f32_e32 v76, v76
	s_waitcnt lgkmcnt(6)
	v_mfma_f32_32x32x16_bf16 v[82:97], v[240:243], v[98:101], v[82:97]
	v_sub_f32_e32 v77, v77, v183
	ds_read_b128 v[232:235], v204 offset:13824
	ds_read_b128 v[236:239], v204 offset:13856
	v_exp_f32_e32 v77, v77
	s_nop 0
	v_cvt_pk_bf16_f32 v193, v76, v77
	s_and_b64 vcc, exec, s[0:1]
	s_cbranch_vccnz .LattA_slow
	s_mul_i32 s12, s36, 0x6400
	s_add_u32 s16, s80, s2
	s_addc_u32 s17, s81, s3
	s_add_u32 s16, s16, 0x30e8a000
	s_addc_u32 s17, s17, 0
	s_waitcnt lgkmcnt(0)
	v_mfma_f32_32x32x16_bf16 v[50:65], v[196:199], v[188:191], v[50:65]
	s_add_i32 m0, s12, s65
	s_nop 0
	global_load_lds_dwordx4 v208, s[16:17]
	v_mfma_f32_32x32x16_bf16 v[34:49], v[216:219], v[188:191], v[34:49]
	s_add_i32 m0, s12, s66
	s_nop 0
	global_load_lds_dwordx4 v209, s[16:17]
	v_mfma_f32_32x32x16_bf16 v[18:33], v[224:227], v[188:191], v[18:33]
	v_max_f32_e32 v152, v82, v83
	v_max3_f32 v152, v152, v84, v85
	s_add_i32 m0, s12, s67
	s_add_i32 s12, s12, s68
	global_load_lds_dwordx4 v210, s[16:17]
	v_mfma_f32_32x32x16_bf16 v[2:17], v[232:235], v[188:191], v[2:17]
	v_max3_f32 v152, v152, v86, v87
	v_max3_f32 v152, v152, v88, v89
	s_add_i32 m0, s12, 0x6000
	s_nop 0
	global_load_lds_dwordx4 v211, s[16:17]
	v_mfma_f32_32x32x16_bf16 v[50:65], v[200:203], v[192:195], v[50:65]
	v_max3_f32 v152, v152, v90, v91
	v_max3_f32 v152, v152, v92, v93
	s_mul_i32 s12, s36, 0x4800
	s_add_i32 s13, s12, 0xffffb800
	s_cmp_lg_u32 s36, 0
	s_cselect_b32 s13, s13, 0x9000
	s_add_i32 s13, s13, 0x12c00
	s_add_u32 s16, s82, s2
	s_addc_u32 s17, s83, s3
	s_add_u32 s16, s16, s28
	s_addc_u32 s17, s17, s29
	s_add_i32 m0, s13, s69
	s_nop 0
	global_load_lds_dwordx4 v212, s[16:17]
	v_mfma_f32_32x32x16_bf16 v[34:49], v[220:223], v[192:195], v[34:49]
	v_max3_f32 v152, v152, v94, v95
	v_max3_f32 v152, v152, v96, v97
	s_add_i32 m0, s13, s70
	s_nop 0
	global_load_lds_dwordx4 v213, s[16:17]
	v_mfma_f32_32x32x16_bf16 v[18:33], v[228:231], v[192:195], v[18:33]
	s_add_i32 m0, s13, s71
	s_nop 0
	global_load_lds_dwordx4 v214, s[16:17]
	v_mfma_f32_32x32x16_bf16 v[2:17], v[236:239], v[192:195], v[2:17]
	v_mov_b32_e32 v153, v152
	s_nop 1
	v_permlane32_swap_b32_e32 v153, v152
	v_max_f32_e32 v152, v152, v153
	s_branch .LattA_join
; #define ATT_DMAK(tile, slot) do { _Pragma("unroll") for (int i = 0; i < 4; ++i) { const int pc = (wv + 8 * i) < 25 ? (wv + 8 * i) : 24; \
;         __builtin_amdgcn_global_load_lds((const unsigned*)((const char*)Kbh + (size_t)(tile) * (64 * 384) + doffK[i]), (LAS unsigned*)(lds + (slot) * KT_BYTES + pc * 1024), 16, 0, 0); } } while (0)
; #define ATT_DMAV(tile, slot) do { _Pragma("unroll") for (int i = 0; i < 3; ++i) { const int pc = (wv + 8 * i) < 18 ? (wv + 8 * i) : 17; \
;         __builtin_amdgcn_global_load_lds((const unsigned*)((const char*)Vbh + (size_t)(tile) * 128 + doffV[i]), (LAS unsigned*)(lds + VRING + (slot) * VT_BYTES + pc * 1024), 16, 0, 0); } } while (0)
; __device__ __forceinline__ void attn_unit(const bf16_t* Qrows  , const bf16_t* Kbh, const bf16_t* Vbh, int nkeys, bf16_t* Orows, LAS unsigned char* lds) {
;     ...
;         if (j + 3 < nt) ATT_DMAK(j + 3, v0);
;         ATT_DMAV(j + 2, v0 == 0 ? 2 : v0 - 1);
.LattA_slow:
	s_waitcnt lgkmcnt(0)
	v_mfma_f32_32x32x16_bf16 v[50:65], v[196:199], v[188:191], v[50:65]
	v_mfma_f32_32x32x16_bf16 v[34:49], v[216:219], v[188:191], v[34:49]
	v_mfma_f32_32x32x16_bf16 v[18:33], v[224:227], v[188:191], v[18:33]
	v_max_f32_e32 v152, v82, v83
	v_max3_f32 v152, v152, v84, v85
	v_mfma_f32_32x32x16_bf16 v[2:17], v[232:235], v[188:191], v[2:17]
	s_and_b64 vcc, exec, s[0:1]
	s_cbranch_vccnz .LattA_v
	s_mul_i32 s12, s36, 0x6400
	s_add_i32 s12, s12, 0
	s_add_u32 s16, s80, s2
	s_addc_u32 s17, s81, s3
	s_add_u32 s16, s16, 0x30e8a000
	s_addc_u32 s17, s17, 0
	s_add_i32 m0, s12, s65
	s_nop 0
	global_load_lds_dwordx4 v208, s[16:17]
	s_add_i32 m0, s12, s66
	s_nop 0
	global_load_lds_dwordx4 v209, s[16:17]
	s_add_i32 m0, s12, s67
	s_add_i32 s12, s12, s68
	global_load_lds_dwordx4 v210, s[16:17]
	s_add_i32 m0, s12, 0x6000
	s_nop 0
	global_load_lds_dwordx4 v211, s[16:17]
.LattA_v:
	v_max3_f32 v152, v152, v86, v87
	v_max3_f32 v152, v152, v88, v89
	v_mfma_f32_32x32x16_bf16 v[50:65], v[200:203], v[192:195], v[50:65]
	v_max3_f32 v152, v152, v90, v91
	v_max3_f32 v152, v152, v92, v93
	v_mfma_f32_32x32x16_bf16 v[34:49], v[220:223], v[192:195], v[34:49]
	v_max3_f32 v152, v152, v94, v95
	v_max3_f32 v152, v152, v96, v97
	v_mfma_f32_32x32x16_bf16 v[18:33], v[228:231], v[192:195], v[18:33]
	v_mfma_f32_32x32x16_bf16 v[2:17], v[236:239], v[192:195], v[2:17]
	v_mov_b32_e32 v153, v152
	s_nop 1
	v_permlane32_swap_b32_e32 v153, v152
	v_max_f32_e32 v152, v152, v153
	s_mul_i32 s12, s36, 0x4800
	s_add_i32 s13, s12, 0xffffb800
	s_cmp_lg_u32 s36, 0
	s_cselect_b32 s13, s13, 0x9000
	s_add_i32 s13, s13, 0
	s_add_i32 s13, s13, 0x12c00
	s_add_u32 s16, s82, s2
	s_addc_u32 s17, s83, s3
	s_add_u32 s16, s16, s28
	s_addc_u32 s17, s17, s29
	s_add_i32 m0, s13, s69
	s_nop 0
	global_load_lds_dwordx4 v212, s[16:17]
	s_add_i32 m0, s13, s70
	s_nop 0
	global_load_lds_dwordx4 v213, s[16:17]
	s_add_i32 m0, s13, s71
	s_nop 0
	global_load_lds_dwordx4 v214, s[16:17]
.LattA_join:
	s_mov_b64 s[12:13], -1
	s_and_b64 vcc, exec, s[0:1]
	s_cbranch_vccz .LBB0_1242
	s_waitcnt vmcnt(0)
	s_mov_b64 s[12:13], 0
